# P10 K-loop: first-iteration SP1 wait skipped (it only retired already-drained loads)
# baseline (speedup 1.0000x reference)
; #define PG8_STAGE(bufoff, gbase, voff) do { _Pragma("unroll") for (int _i = 0; _i < 2; ++_i) \
;         __builtin_amdgcn_global_load_lds((const unsigned*)((const char*)(gbase) + (voff)[_i]), (PG8_LAS unsigned*)(lds + (bufoff) + ldsw + _i * 8192), 16, 0, 0); } while (0)
; #define PG8_LDA(dst, b, h) do { _Pragma("unroll") for (int m = 0; m < 4; ++m) _Pragma("unroll") for (int k = 0; k < 2; ++k) dst[m][k] = *(const PG8_LAS bf16x8*)(lds + PG8_SA(b, h) + aoff + m * 2048 + k * 1024); } while (0)
; #define PG8_LDB(dst, b, h) do { _Pragma("unroll") for (int n = 0; n < 2; ++n) _Pragma("unroll") for (int k = 0; k < 2; ++k) dst[n][k] = *(const PG8_LAS bf16x8*)(lds + PG8_SB(b, h) + boff + n * 2048 + k * 1024); } while (0)
; #define PG8_WAIT_V(n) asm volatile("s_waitcnt vmcnt(" #n ")" ::: "memory")
; #define PG8_WAIT_L(n) asm volatile("s_waitcnt lgkmcnt(" #n ")" ::: "memory")
; #define PG8_BAR __builtin_amdgcn_s_barrier()
; #define PG8_SCHED __builtin_amdgcn_sched_barrier(0)
; template <class Epi, class Sched, bool ALIGN_EPI = false, bool SP2 = false, bool F8 = false, bool GATHER = false>
; __device__ __forceinline__ void gemm_phase(PG8_LAS unsigned char* lds, const Gemm g, const Sched& S, const Epi& E) {
;     ...
;         for (int t = 0; t < nt; t += 2) {
;             const bool last = (t == nt - 2);
;             const char* a1 = cA + (size_t)(t + 1) * kstep;
;             const char* a2 = last ? nA : cA + (size_t)(t + 2) * kstep; const char* b2 = last ? nB : cB + (size_t)(t + 2) * kstep;
;             const char* a3 = a2 + kstep; const char* b3 = b2 + kstep;
;             unsigned s0[2], s1[2];
; #pragma unroll
;             for (int _i = 0; _i < 2; ++_i) { s0[_i] = last ? nvo[0][_i] : vo[0][_i]; s1[_i] = last ? nvo[1][_i] : vo[1][_i]; }
;             if (last && has_next) S.a_ready(nxt);
;             if constexpr (SP2) {
;             PG8_LDB(B0, 0, 0); PG8_LDB(B1, 0, 1); PG8_SCHED; PG8_LDA(At, 0, 0); PG8_STAGE(PG8_SA(1, 1), a1, vo[1]);
;             PG8_WAIT_V(8); PG8_WAIT_L(0); PG8_BAR; PG8_MMA(0, 0, At, B0); PG8_MMA(0, 1, At, B1); PG8_BAR; PG8_SCHED;
;             PG8_LDA(At, 0, 1); PG8_STAGE(PG8_SB(0, 0), b2, voffB); PG8_STAGE(PG8_SB(0, 1), b2 + hstep, voffB); PG8_STAGE(PG8_SA(0, 0), a2, s0);
;             PG8_WAIT_V(8); PG8_WAIT_L(0); PG8_BAR; PG8_MMA(1, 0, At, B0); PG8_MMA(1, 1, At, B1); PG8_BAR; PG8_SCHED;
.LBB0_1073:
	ds_read_b128 v[26:29], v196
	ds_read_b128 v[30:33], v196 offset:1024
	ds_read_b128 v[18:21], v196 offset:2048
	ds_read_b128 v[22:25], v196 offset:3072
	ds_read_b128 v[10:13], v197
	ds_read_b128 v[14:17], v197 offset:1024
	ds_read_b128 v[2:5], v197 offset:2048
	ds_read_b128 v[6:9], v197 offset:3072
	s_add_u32 s54, s30, s4
	s_addc_u32 s55, s31, s5
	s_add_u32 s56, s54, 0x30200100
	s_addc_u32 s57, s55, 0
	s_add_u32 s72, s69, s4
	s_addc_u32 s73, s70, s5
	s_cmpk_eq_i32 s4, 0x700
	s_cselect_b64 vcc, -1, 0
	s_and_b64 s[54:55], vcc, exec
	v_cndmask_b32_e32 v166, v204, v200, vcc
	s_cselect_b32 s57, s13, s57
	s_cselect_b32 s56, s12, s56
	v_cndmask_b32_e32 v171, v170, v202, vcc
	v_cndmask_b32_e32 v238, v168, v201, vcc
	v_cndmask_b32_e32 v173, v172, v203, vcc
	s_cselect_b32 s55, s49, s73
	s_cselect_b32 s54, s68, s72
	v_lshl_add_u64 v[230:231], v[176:177], 0, s[4:5]
	s_add_i32 m0, s11, 0xc000
	ds_read_b128 v[178:181], v198
	ds_read_b128 v[182:185], v198 offset:1024
	ds_read_b128 v[206:209], v198 offset:2048
	ds_read_b128 v[210:213], v198 offset:3072
	ds_read_b128 v[214:217], v198 offset:4096
	ds_read_b128 v[218:221], v198 offset:5120
	ds_read_b128 v[222:225], v198 offset:6144
	ds_read_b128 v[226:229], v198 offset:7168
	global_load_lds_dwordx4 v[230:231], off
	v_lshl_add_u64 v[230:231], v[174:175], 0, s[4:5]
	s_add_i32 m0, s11, 0xe000
	s_nop 0
	global_load_lds_dwordx4 v[230:231], off
	s_cmp_eq_u32 s71, -2
	s_cbranch_scc1 .Lw10_skip
	s_waitcnt vmcnt(8)
.Lw10_skip:
	s_waitcnt lgkmcnt(0)
	s_barrier
	s_setprio 1
	s_waitcnt lgkmcnt(0)
	v_mfma_scale_f32_16x16x128_f8f6f4 v[158:161], v[26:33], v[178:185], v[158:161], v199, v199 op_sel_hi:[0,0,0]
	v_mfma_scale_f32_16x16x128_f8f6f4 v[154:157], v[18:25], v[178:185], v[154:157], v199, v199 op_sel_hi:[0,0,0]
	v_mfma_scale_f32_16x16x128_f8f6f4 v[146:149], v[26:33], v[206:213], v[146:149], v199, v199 op_sel_hi:[0,0,0]
	v_mfma_scale_f32_16x16x128_f8f6f4 v[138:141], v[18:25], v[206:213], v[138:141], v199, v199 op_sel_hi:[0,0,0]
	v_mfma_scale_f32_16x16x128_f8f6f4 v[130:133], v[26:33], v[214:221], v[130:133], v199, v199 op_sel_hi:[0,0,0]
	v_mfma_scale_f32_16x16x128_f8f6f4 v[122:125], v[18:25], v[214:221], v[122:125], v199, v199 op_sel_hi:[0,0,0]
	v_mfma_scale_f32_16x16x128_f8f6f4 v[114:117], v[26:33], v[222:229], v[114:117], v199, v199 op_sel_hi:[0,0,0]
	v_mfma_scale_f32_16x16x128_f8f6f4 v[106:109], v[18:25], v[222:229], v[106:109], v199, v199 op_sel_hi:[0,0,0]
	s_setprio 0
	s_setprio 1
	v_mfma_scale_f32_16x16x128_f8f6f4 v[150:153], v[10:17], v[178:185], v[150:153], v199, v199 op_sel_hi:[0,0,0]
	v_mfma_scale_f32_16x16x128_f8f6f4 v[142:145], v[2:9], v[178:185], v[142:145], v199, v199 op_sel_hi:[0,0,0]
	v_mfma_scale_f32_16x16x128_f8f6f4 v[134:137], v[10:17], v[206:213], v[134:137], v199, v199 op_sel_hi:[0,0,0]
	v_mfma_scale_f32_16x16x128_f8f6f4 v[126:129], v[2:9], v[206:213], v[126:129], v199, v199 op_sel_hi:[0,0,0]
	v_mfma_scale_f32_16x16x128_f8f6f4 v[118:121], v[10:17], v[214:221], v[118:121], v199, v199 op_sel_hi:[0,0,0]
	v_mfma_scale_f32_16x16x128_f8f6f4 v[110:113], v[2:9], v[214:221], v[110:113], v199, v199 op_sel_hi:[0,0,0]
	v_mfma_scale_f32_16x16x128_f8f6f4 v[102:105], v[10:17], v[222:229], v[102:105], v199, v199 op_sel_hi:[0,0,0]
	v_mfma_scale_f32_16x16x128_f8f6f4 v[98:101], v[2:9], v[222:229], v[98:101], v199, v199 op_sel_hi:[0,0,0]
	s_setprio 0
	s_barrier
	s_add_i32 s72, s60, s1
	v_lshl_add_u64 v[178:179], s[54:55], 0, v[164:165]
	s_mov_b32 m0, s72
	ds_read_b128 v[206:209], v198 offset:16384
	ds_read_b128 v[210:213], v198 offset:17408
	ds_read_b128 v[214:217], v198 offset:18432
	ds_read_b128 v[218:221], v198 offset:19456
	ds_read_b128 v[222:225], v198 offset:20480
	ds_read_b128 v[226:229], v198 offset:21504
	ds_read_b128 v[230:233], v198 offset:22528
	ds_read_b128 v[234:237], v198 offset:23552
	global_load_lds_dwordx4 v[178:179], off
	s_add_i32 m0, s72, 0x2000
	s_add_u32 s72, s54, 0x40000
	v_lshl_add_u64 v[180:181], s[54:55], 0, v[162:163]
	s_addc_u32 s73, s55, 0
	s_add_i32 s74, s61, s1
	global_load_lds_dwordx4 v[180:181], off
	v_lshl_add_u64 v[182:183], s[72:73], 0, v[164:165]
	s_mov_b32 m0, s74
	v_mov_b32_e32 v239, v167
	global_load_lds_dwordx4 v[182:183], off
	v_lshl_add_u64 v[182:183], s[72:73], 0, v[162:163]
	s_add_i32 m0, s74, 0x2000
	v_lshl_add_u64 v[184:185], s[56:57], 0, v[166:167]
	global_load_lds_dwordx4 v[182:183], off
	s_mov_b32 m0, s11
	v_lshl_add_u64 v[182:183], s[56:57], 0, v[238:239]
	global_load_lds_dwordx4 v166, s[56:57]
	s_mov_b32 m0, s33
	s_nop 0
	global_load_lds_dwordx4 v238, s[56:57]
	s_waitcnt vmcnt(8)
	s_waitcnt lgkmcnt(0)
	s_barrier
	s_setprio 1
	s_waitcnt lgkmcnt(0)
	v_mfma_scale_f32_16x16x128_f8f6f4 v[94:97], v[26:33], v[206:213], v[94:97], v199, v199 op_sel_hi:[0,0,0]
	v_mfma_scale_f32_16x16x128_f8f6f4 v[90:93], v[18:25], v[206:213], v[90:93], v199, v199 op_sel_hi:[0,0,0]
	v_mfma_scale_f32_16x16x128_f8f6f4 v[82:85], v[26:33], v[214:221], v[82:85], v199, v199 op_sel_hi:[0,0,0]
	v_mfma_scale_f32_16x16x128_f8f6f4 v[74:77], v[18:25], v[214:221], v[74:77], v199, v199 op_sel_hi:[0,0,0]
	v_mfma_scale_f32_16x16x128_f8f6f4 v[66:69], v[26:33], v[222:229], v[66:69], v199, v199 op_sel_hi:[0,0,0]
	v_mfma_scale_f32_16x16x128_f8f6f4 v[58:61], v[18:25], v[222:229], v[58:61], v199, v199 op_sel_hi:[0,0,0]
	v_mfma_scale_f32_16x16x128_f8f6f4 v[50:53], v[26:33], v[230:237], v[50:53], v199, v199 op_sel_hi:[0,0,0]
	v_mfma_scale_f32_16x16x128_f8f6f4 v[42:45], v[18:25], v[230:237], v[42:45], v199, v199 op_sel_hi:[0,0,0]
	s_setprio 0
	s_setprio 1
	v_mfma_scale_f32_16x16x128_f8f6f4 v[86:89], v[10:17], v[206:213], v[86:89], v199, v199 op_sel_hi:[0,0,0]
	v_mfma_scale_f32_16x16x128_f8f6f4 v[78:81], v[2:9], v[206:213], v[78:81], v199, v199 op_sel_hi:[0,0,0]
	v_mfma_scale_f32_16x16x128_f8f6f4 v[70:73], v[10:17], v[214:221], v[70:73], v199, v199 op_sel_hi:[0,0,0]
	v_mfma_scale_f32_16x16x128_f8f6f4 v[62:65], v[2:9], v[214:221], v[62:65], v199, v199 op_sel_hi:[0,0,0]
	v_mfma_scale_f32_16x16x128_f8f6f4 v[54:57], v[10:17], v[222:229], v[54:57], v199, v199 op_sel_hi:[0,0,0]
	v_mfma_scale_f32_16x16x128_f8f6f4 v[46:49], v[2:9], v[222:229], v[46:49], v199, v199 op_sel_hi:[0,0,0]
	v_mfma_scale_f32_16x16x128_f8f6f4 v[38:41], v[10:17], v[230:237], v[38:41], v199, v199 op_sel_hi:[0,0,0]
	v_mfma_scale_f32_16x16x128_f8f6f4 v[34:37], v[2:9], v[230:237], v[34:37], v199, v199 op_sel_hi:[0,0,0]
	s_setprio 0
	s_barrier
; #define PG8_STAGE(bufoff, gbase, voff) do { _Pragma("unroll") for (int _i = 0; _i < 2; ++_i) \
;         __builtin_amdgcn_global_load_lds((const unsigned*)((const char*)(gbase) + (voff)[_i]), (PG8_LAS unsigned*)(lds + (bufoff) + ldsw + _i * 8192), 16, 0, 0); } while (0)
; #define PG8_LDA(dst, b, h) do { _Pragma("unroll") for (int m = 0; m < 4; ++m) _Pragma("unroll") for (int k = 0; k < 2; ++k) dst[m][k] = *(const PG8_LAS bf16x8*)(lds + PG8_SA(b, h) + aoff + m * 2048 + k * 1024); } while (0)
; #define PG8_LDB(dst, b, h) do { _Pragma("unroll") for (int n = 0; n < 2; ++n) _Pragma("unroll") for (int k = 0; k < 2; ++k) dst[n][k] = *(const PG8_LAS bf16x8*)(lds + PG8_SB(b, h) + boff + n * 2048 + k * 1024); } while (0)
; #define PG8_WAIT_V(n) asm volatile("s_waitcnt vmcnt(" #n ")" ::: "memory")
; #define PG8_WAIT_L(n) asm volatile("s_waitcnt lgkmcnt(" #n ")" ::: "memory")
; #define PG8_BAR __builtin_amdgcn_s_barrier()
; #define PG8_SCHED __builtin_amdgcn_sched_barrier(0)
; template <class Epi, class Sched, bool ALIGN_EPI = false, bool SP2 = false, bool F8 = false, bool GATHER = false>
; __device__ __forceinline__ void gemm_phase(PG8_LAS unsigned char* lds, const Gemm g, const Sched& S, const Epi& E) {
;     ...
;             PG8_LDB(B0, 1, 0); PG8_LDB(B1, 1, 1); PG8_SCHED; PG8_LDA(At, 1, 0); PG8_STAGE(PG8_SA(0, 1), a2, s1);
;             PG8_WAIT_V(8); PG8_WAIT_L(0); PG8_BAR; PG8_MMA(0, 0, At, B0); PG8_MMA(0, 1, At, B1); PG8_BAR; PG8_SCHED;
;             PG8_LDA(At, 1, 1); PG8_STAGE(PG8_SB(1, 0), b3, voffB); PG8_STAGE(PG8_SB(1, 1), b3 + hstep, voffB); PG8_STAGE(PG8_SA(1, 0), a3, s0);
;             PG8_WAIT_V(8); PG8_WAIT_L(0); PG8_BAR; PG8_MMA(1, 0, At, B0); PG8_MMA(1, 1, At, B1); PG8_BAR; PG8_SCHED;
;     ...
;         if constexpr (F8) asm volatile("s_nop 15\n\ts_nop 7" ::: "memory");
;         if constexpr (ALIGN_EPI) { if (wr == 0) PG8_BAR; }
	s_add_i32 s72, 0, 0x18000
	s_add_i32 s73, 0, 0x1c000
	v_add_u32_e32 v14, s72, v194
	v_add_u32_e32 v30, s73, v194
	ds_read_b128 v[2:5], v14
	ds_read_b128 v[6:9], v14 offset:1024
	ds_read_b128 v[10:13], v14 offset:2048
	ds_read_b128 v[14:17], v14 offset:3072
	ds_read_b128 v[18:21], v30
	ds_read_b128 v[22:25], v30 offset:1024
	ds_read_b128 v[26:29], v30 offset:2048
	ds_read_b128 v[30:33], v30 offset:3072
	s_mov_b32 m0, s34
	ds_read_b128 v[206:209], v198 offset:32768
	ds_read_b128 v[210:213], v198 offset:33792
	ds_read_b128 v[214:217], v198 offset:34816
	ds_read_b128 v[218:221], v198 offset:35840
	ds_read_b128 v[222:225], v198 offset:36864
	ds_read_b128 v[226:229], v198 offset:37888
	ds_read_b128 v[230:233], v198 offset:38912
	ds_read_b128 v[234:237], v198 offset:39936
	global_load_lds_dwordx4 v171, s[56:57]
	s_mov_b32 m0, s35
	s_nop 0
	global_load_lds_dwordx4 v173, s[56:57]
	s_waitcnt vmcnt(8)
	s_waitcnt lgkmcnt(0)
	s_barrier
	s_setprio 1
	s_waitcnt lgkmcnt(0)
	v_mfma_scale_f32_16x16x128_f8f6f4 v[158:161], v[2:9], v[206:213], v[158:161], v199, v199 op_sel_hi:[0,0,0]
	v_mfma_scale_f32_16x16x128_f8f6f4 v[154:157], v[10:17], v[206:213], v[154:157], v199, v199 op_sel_hi:[0,0,0]
	v_mfma_scale_f32_16x16x128_f8f6f4 v[146:149], v[2:9], v[214:221], v[146:149], v199, v199 op_sel_hi:[0,0,0]
	v_mfma_scale_f32_16x16x128_f8f6f4 v[138:141], v[10:17], v[214:221], v[138:141], v199, v199 op_sel_hi:[0,0,0]
	v_mfma_scale_f32_16x16x128_f8f6f4 v[130:133], v[2:9], v[222:229], v[130:133], v199, v199 op_sel_hi:[0,0,0]
	v_mfma_scale_f32_16x16x128_f8f6f4 v[122:125], v[10:17], v[222:229], v[122:125], v199, v199 op_sel_hi:[0,0,0]
	v_mfma_scale_f32_16x16x128_f8f6f4 v[114:117], v[2:9], v[230:237], v[114:117], v199, v199 op_sel_hi:[0,0,0]
	v_mfma_scale_f32_16x16x128_f8f6f4 v[106:109], v[10:17], v[230:237], v[106:109], v199, v199 op_sel_hi:[0,0,0]
	s_setprio 0
	s_setprio 1
	v_mfma_scale_f32_16x16x128_f8f6f4 v[150:153], v[18:25], v[206:213], v[150:153], v199, v199 op_sel_hi:[0,0,0]
	v_mfma_scale_f32_16x16x128_f8f6f4 v[142:145], v[26:33], v[206:213], v[142:145], v199, v199 op_sel_hi:[0,0,0]
	v_mfma_scale_f32_16x16x128_f8f6f4 v[134:137], v[18:25], v[214:221], v[134:137], v199, v199 op_sel_hi:[0,0,0]
	v_mfma_scale_f32_16x16x128_f8f6f4 v[126:129], v[26:33], v[214:221], v[126:129], v199, v199 op_sel_hi:[0,0,0]
	v_mfma_scale_f32_16x16x128_f8f6f4 v[118:121], v[18:25], v[222:229], v[118:121], v199, v199 op_sel_hi:[0,0,0]
	v_mfma_scale_f32_16x16x128_f8f6f4 v[110:113], v[26:33], v[222:229], v[110:113], v199, v199 op_sel_hi:[0,0,0]
	v_mfma_scale_f32_16x16x128_f8f6f4 v[102:105], v[18:25], v[230:237], v[102:105], v199, v199 op_sel_hi:[0,0,0]
	v_mfma_scale_f32_16x16x128_f8f6f4 v[98:101], v[26:33], v[230:237], v[98:101], v199, v199 op_sel_hi:[0,0,0]
	s_setprio 0
	s_barrier
	s_add_i32 s56, s72, s1
	v_lshl_add_u64 v[178:179], v[178:179], 0, s[22:23]
	s_mov_b32 m0, s56
	ds_read_b128 v[206:209], v198 offset:49152
	ds_read_b128 v[210:213], v198 offset:50176
	ds_read_b128 v[214:217], v198 offset:51200
	ds_read_b128 v[218:221], v198 offset:52224
	ds_read_b128 v[222:225], v198 offset:53248
	ds_read_b128 v[226:229], v198 offset:54272
	ds_read_b128 v[230:233], v198 offset:55296
	ds_read_b128 v[234:237], v198 offset:56320
	global_load_lds_dwordx4 v[178:179], off
	s_add_i32 m0, s56, 0x2000
	s_add_u32 s54, s54, 0x40080
	v_lshl_add_u64 v[178:179], v[180:181], 0, s[22:23]
	s_addc_u32 s55, s55, 0
	s_add_i32 s56, s73, s1
	global_load_lds_dwordx4 v[178:179], off
	v_lshl_add_u64 v[178:179], s[54:55], 0, v[164:165]
	s_mov_b32 m0, s56
	s_nop 0
	global_load_lds_dwordx4 v[178:179], off
	v_lshl_add_u64 v[178:179], s[54:55], 0, v[162:163]
	s_add_i32 m0, s56, 0x2000
	s_nop 0
	global_load_lds_dwordx4 v[178:179], off
	v_lshl_add_u64 v[178:179], v[184:185], 0, s[22:23]
	s_mov_b32 m0, s58
	s_nop 0
	global_load_lds_dwordx4 v[178:179], off
	v_lshl_add_u64 v[178:179], v[182:183], 0, s[22:23]
	s_mov_b32 m0, s59
	s_nop 0
	global_load_lds_dwordx4 v[178:179], off
	s_waitcnt vmcnt(8)
	s_waitcnt lgkmcnt(0)
	s_barrier
	s_setprio 1
	s_waitcnt lgkmcnt(0)
	v_mfma_scale_f32_16x16x128_f8f6f4 v[94:97], v[2:9], v[206:213], v[94:97], v199, v199 op_sel_hi:[0,0,0]
	v_mfma_scale_f32_16x16x128_f8f6f4 v[90:93], v[10:17], v[206:213], v[90:93], v199, v199 op_sel_hi:[0,0,0]
	v_mfma_scale_f32_16x16x128_f8f6f4 v[82:85], v[2:9], v[214:221], v[82:85], v199, v199 op_sel_hi:[0,0,0]
	v_mfma_scale_f32_16x16x128_f8f6f4 v[74:77], v[10:17], v[214:221], v[74:77], v199, v199 op_sel_hi:[0,0,0]
	v_mfma_scale_f32_16x16x128_f8f6f4 v[66:69], v[2:9], v[222:229], v[66:69], v199, v199 op_sel_hi:[0,0,0]
	v_mfma_scale_f32_16x16x128_f8f6f4 v[58:61], v[10:17], v[222:229], v[58:61], v199, v199 op_sel_hi:[0,0,0]
	v_mfma_scale_f32_16x16x128_f8f6f4 v[50:53], v[2:9], v[230:237], v[50:53], v199, v199 op_sel_hi:[0,0,0]
	v_mfma_scale_f32_16x16x128_f8f6f4 v[42:45], v[10:17], v[230:237], v[42:45], v199, v199 op_sel_hi:[0,0,0]
	s_setprio 0
	s_setprio 1
	v_mfma_scale_f32_16x16x128_f8f6f4 v[86:89], v[18:25], v[206:213], v[86:89], v199, v199 op_sel_hi:[0,0,0]
	v_mfma_scale_f32_16x16x128_f8f6f4 v[78:81], v[26:33], v[206:213], v[78:81], v199, v199 op_sel_hi:[0,0,0]
	v_mfma_scale_f32_16x16x128_f8f6f4 v[70:73], v[18:25], v[214:221], v[70:73], v199, v199 op_sel_hi:[0,0,0]
	v_mfma_scale_f32_16x16x128_f8f6f4 v[62:65], v[26:33], v[214:221], v[62:65], v199, v199 op_sel_hi:[0,0,0]
	v_mfma_scale_f32_16x16x128_f8f6f4 v[54:57], v[18:25], v[222:229], v[54:57], v199, v199 op_sel_hi:[0,0,0]
	v_mfma_scale_f32_16x16x128_f8f6f4 v[46:49], v[26:33], v[222:229], v[46:49], v199, v199 op_sel_hi:[0,0,0]
	v_mfma_scale_f32_16x16x128_f8f6f4 v[38:41], v[18:25], v[230:237], v[38:41], v199, v199 op_sel_hi:[0,0,0]
	v_mfma_scale_f32_16x16x128_f8f6f4 v[34:37], v[26:33], v[230:237], v[34:37], v199, v199 op_sel_hi:[0,0,0]
	s_setprio 0
	s_barrier
	s_add_i32 s71, s71, 2
	s_add_u32 s4, s4, 0x100
	s_addc_u32 s5, s5, 0
	s_cmp_gt_u32 s71, 13
	s_cbranch_scc0 .LBB0_1073
	s_nop 15
	s_nop 7
	s_and_b64 vcc, exec, s[36:37]
	s_cbranch_vccz .LBB0_1076
	s_barrier
